# v59 + NA: per-lane half-row partial sums in the loop, one lane exchange of l per unit
# baseline (speedup 1.0000x reference)
.LBB0_799:
	v_cndmask_b32_e64 v65, v65, v206, s[58:59]
	v_mul_f32_e32 v65, 0xbe0293ee, v65
	v_fmamk_f32 v67, v113, 0x3e0293ee, v65
	v_exp_f32_e32 v83, v67
	v_fmamk_f32 v67, v112, 0x3e0293ee, v65
	v_exp_f32_e32 v85, v67
	v_fmamk_f32 v67, v111, 0x3e0293ee, v65
	v_exp_f32_e32 v81, v67
	v_fmamk_f32 v67, v110, 0x3e0293ee, v65
	v_exp_f32_e32 v87, v67
	v_fmamk_f32 v67, v109, 0x3e0293ee, v65
	v_exp_f32_e32 v89, v67
	v_fmamk_f32 v67, v108, 0x3e0293ee, v65
	v_exp_f32_e32 v91, v67
	v_fmamk_f32 v67, v107, 0x3e0293ee, v65
	v_exp_f32_e32 v93, v67
	v_fmamk_f32 v67, v106, 0x3e0293ee, v65
	v_exp_f32_e32 v95, v67
	v_fmamk_f32 v67, v105, 0x3e0293ee, v65
	v_exp_f32_e32 v105, v67
	v_fmamk_f32 v67, v104, 0x3e0293ee, v65
	v_exp_f32_e32 v107, v67
	v_fmamk_f32 v67, v103, 0x3e0293ee, v65
	v_exp_f32_e32 v77, v67
	v_fmamk_f32 v67, v102, 0x3e0293ee, v65
	v_exp_f32_e32 v103, v67
	v_fmamk_f32 v67, v99, 0x3e0293ee, v65
	v_exp_f32_e32 v99, v67
	v_fmamk_f32 v67, v98, 0x3e0293ee, v65
	v_exp_f32_e32 v109, v67
	v_fmamk_f32 v67, v97, 0x3e0293ee, v65
	v_exp_f32_e32 v75, v67
	v_fmamk_f32 v67, v96, 0x3e0293ee, v65
	v_exp_f32_e32 v97, v67
	v_fmamk_f32 v67, v79, 0x3e0293ee, v65
	v_fmamk_f32 v69, v125, 0x3e0293ee, v65
	v_fmamk_f32 v70, v124, 0x3e0293ee, v65
	v_fmamk_f32 v73, v123, 0x3e0293ee, v65
	v_fmamk_f32 v78, v122, 0x3e0293ee, v65
	v_fmamk_f32 v79, v121, 0x3e0293ee, v65
	v_fmamk_f32 v80, v120, 0x3e0293ee, v65
	v_fmamk_f32 v72, v72, 0x3e0293ee, v65
	v_fmamk_f32 v71, v71, 0x3e0293ee, v65
	v_fmamk_f32 v82, v119, 0x3e0293ee, v65
	v_fmamk_f32 v76, v118, 0x3e0293ee, v65
	v_fmamk_f32 v84, v117, 0x3e0293ee, v65
	v_fmamk_f32 v86, v116, 0x3e0293ee, v65
	v_fmamk_f32 v88, v115, 0x3e0293ee, v65
	v_fmamk_f32 v74, v114, 0x3e0293ee, v65
	v_fmac_f32_e32 v65, 0x3e0293ee, v64
	v_exp_f32_e32 v96, v65
	v_exp_f32_e32 v74, v74
	v_exp_f32_e32 v94, v72
	v_exp_f32_e32 v92, v80
	v_exp_f32_e32 v108, v88
	v_exp_f32_e32 v90, v79
	v_exp_f32_e32 v98, v86
	v_exp_f32_e32 v88, v78
	v_exp_f32_e32 v102, v84
	v_exp_f32_e32 v86, v73
	v_exp_f32_e32 v76, v76
	v_exp_f32_e32 v104, v71
	v_exp_f32_e32 v80, v70
	v_pk_add_f32 v[70:71], v[96:97], v[74:75]
	v_pk_add_f32 v[72:73], v[94:95], v[92:93]
	v_exp_f32_e32 v106, v82
	v_exp_f32_e32 v84, v69
	v_pk_add_f32 v[70:71], v[108:109], v[70:71]
	v_pk_add_f32 v[72:73], v[90:91], v[72:73]
	v_exp_f32_e32 v82, v67
	v_pk_add_f32 v[70:71], v[98:99], v[70:71]
	v_pk_add_f32 v[72:73], v[88:89], v[72:73]
	v_pk_add_f32 v[70:71], v[102:103], v[70:71]
	v_pk_add_f32 v[72:73], v[86:87], v[72:73]
	v_pk_add_f32 v[70:71], v[76:77], v[70:71]
	v_pk_add_f32 v[72:73], v[80:81], v[72:73]
	v_pk_add_f32 v[70:71], v[106:107], v[70:71]
	v_pk_add_f32 v[72:73], v[84:85], v[72:73]
	v_pk_add_f32 v[70:71], v[104:105], v[70:71]
	v_pk_add_f32 v[72:73], v[82:83], v[72:73]
	s_lshl_b64 s[2:3], s[78:79], 12
	v_pk_add_f32 v[70:71], v[72:73], v[70:71]
	s_add_u32 s6, s35, s2
	v_pk_add_f32 v[70:71], v[70:71], v[70:71] op_sel:[0,1] op_sel_hi:[1,0]
	s_addc_u32 s7, s36, s3
	s_lshl_b32 s2, s15, 7
	v_mov_b32_e32 v69, v70
	s_ashr_i32 s3, s2, 31
	s_nop 0
	v_permlane32_swap_b32_e32 v70, v69
	s_lshl_b64 s[2:3], s[2:3], 1
	v_mov_b32_e32 v64, v187
	s_nop 1
	v_permlane32_swap_b32_e32 v187, v64
	v_add_f32_e32 v187, v187, v64
	v_mul_f32_e32 v64, v162, v187
	v_add_f32_e32 v68, v100, v101
	v_mov_b32_e32 v65, v70
	s_add_u32 s6, s6, s2
	v_pk_add_f32 v[64:65], v[64:65], v[68:69]
	s_addc_u32 s7, s7, s3
	v_fmac_f32_e32 v65, v64, v66
	v_cvt_pk_bf16_f32 v66, v97, v75
	v_cvt_pk_bf16_f32 v67, v109, v99
	v_cvt_pk_bf16_f32 v68, v103, v77
	v_cvt_pk_bf16_f32 v69, v107, v105
	v_cvt_pk_bf16_f32 v70, v95, v93
	v_cvt_pk_bf16_f32 v71, v91, v89
	v_cvt_pk_bf16_f32 v72, v87, v81
	v_cvt_pk_bf16_f32 v73, v85, v83
	v_cvt_pk_bf16_f32 v74, v96, v74
	v_cvt_pk_bf16_f32 v75, v108, v98
	v_cvt_pk_bf16_f32 v76, v102, v76
	v_cvt_pk_bf16_f32 v77, v106, v104
	v_cvt_pk_bf16_f32 v78, v94, v92
	v_cvt_pk_bf16_f32 v79, v90, v88
	v_cvt_pk_bf16_f32 v80, v86, v80
	v_cvt_pk_bf16_f32 v81, v84, v82
	s_cmp_lg_u32 0, -1
	s_cselect_b32 s2, 0, 0
	s_addk_i32 s2, 0x4000
	v_add_u32_e32 v64, s2, v181
	ds_read_b64_tr_b16 v[82:83], v64 offset:0
	ds_read_b64_tr_b16 v[84:85], v64 offset:0x800
	ds_read_b64_tr_b16 v[86:87], v64 offset:0x1000
	ds_read_b64_tr_b16 v[88:89], v64 offset:0x1800
	ds_read_b64_tr_b16 v[90:91], v64 offset:0x2000
	ds_read_b64_tr_b16 v[92:93], v64 offset:0x2800
	ds_read_b64_tr_b16 v[94:95], v64 offset:0x3000
	ds_read_b64_tr_b16 v[96:97], v64 offset:0x3800
	s_waitcnt lgkmcnt(0)
	s_nop 0
	v_mfma_f32_32x32x16_bf16 v[48:63], v[82:85], v[66:69], v[48:63]
	ds_read_b64_tr_b16 v[82:83], v64 offset:0x200
	ds_read_b64_tr_b16 v[84:85], v64 offset:0xa00
	v_mfma_f32_32x32x16_bf16 v[48:63], v[86:89], v[70:73], v[48:63]
	ds_read_b64_tr_b16 v[86:87], v64 offset:0x1200
	ds_read_b64_tr_b16 v[88:89], v64 offset:0x1a00
	v_mfma_f32_32x32x16_bf16 v[48:63], v[90:93], v[74:77], v[48:63]
	ds_read_b64_tr_b16 v[90:91], v64 offset:0x2200
	ds_read_b64_tr_b16 v[92:93], v64 offset:0x2a00
	v_mfma_f32_32x32x16_bf16 v[48:63], v[94:97], v[78:81], v[48:63]
	ds_read_b64_tr_b16 v[94:95], v64 offset:0x3200
	ds_read_b64_tr_b16 v[96:97], v64 offset:0x3a00
	s_waitcnt lgkmcnt(0)
	v_mfma_f32_32x32x16_bf16 v[32:47], v[82:85], v[66:69], v[32:47]
	ds_read_b64_tr_b16 v[82:83], v64 offset:0x400
	ds_read_b64_tr_b16 v[84:85], v64 offset:0xc00
	v_mfma_f32_32x32x16_bf16 v[32:47], v[86:89], v[70:73], v[32:47]
	ds_read_b64_tr_b16 v[86:87], v64 offset:0x1400
	ds_read_b64_tr_b16 v[88:89], v64 offset:0x1c00
	v_mfma_f32_32x32x16_bf16 v[32:47], v[90:93], v[74:77], v[32:47]
	ds_read_b64_tr_b16 v[90:91], v64 offset:0x2400
	ds_read_b64_tr_b16 v[92:93], v64 offset:0x2c00
	v_mfma_f32_32x32x16_bf16 v[32:47], v[94:97], v[78:81], v[32:47]
	ds_read_b64_tr_b16 v[94:95], v64 offset:0x3400
	ds_read_b64_tr_b16 v[96:97], v64 offset:0x3c00
	s_waitcnt lgkmcnt(0)
	v_mfma_f32_32x32x16_bf16 v[16:31], v[82:85], v[66:69], v[16:31]
	ds_read_b64_tr_b16 v[82:83], v64 offset:0x600
	ds_read_b64_tr_b16 v[84:85], v64 offset:0xe00
	v_mfma_f32_32x32x16_bf16 v[16:31], v[86:89], v[70:73], v[16:31]
	ds_read_b64_tr_b16 v[86:87], v64 offset:0x1600
	ds_read_b64_tr_b16 v[88:89], v64 offset:0x1e00
	v_mfma_f32_32x32x16_bf16 v[16:31], v[90:93], v[74:77], v[16:31]
	ds_read_b64_tr_b16 v[90:91], v64 offset:0x2600
	ds_read_b64_tr_b16 v[92:93], v64 offset:0x2e00
	v_mfma_f32_32x32x16_bf16 v[16:31], v[94:97], v[78:81], v[16:31]
	ds_read_b64_tr_b16 v[94:95], v64 offset:0x3600
	ds_read_b64_tr_b16 v[96:97], v64 offset:0x3e00
	s_waitcnt lgkmcnt(0)
	v_mfma_f32_32x32x16_bf16 v[0:15], v[82:85], v[66:69], v[0:15]
	v_rcp_f32_e32 v67, v65
	v_mbcnt_lo_u32_b32 v66, -1, 0
	v_mbcnt_hi_u32_b32 v66, -1, v66
	s_add_i32 s12, s12, 1
	v_add_u32_e32 v64, s80, v66
	v_ashrrev_i32_e32 v64, 1, v64
	v_mul_f32_e32 v48, v67, v48
	v_mul_f32_e32 v49, v67, v49
	v_bfi_b32 v64, s84, v64, v66
	v_cvt_pk_bf16_f32 v48, v48, v49
	v_mul_f32_e32 v49, v67, v50
	v_mul_f32_e32 v50, v67, v51
	v_ashrrev_i32_e32 v65, 31, v64
	v_cvt_pk_bf16_f32 v49, v49, v50
	v_mul_f32_e32 v50, v67, v52
	v_mul_f32_e32 v51, v67, v53
	v_lshlrev_b64 v[64:65], 12, v[64:65]
	v_lshrrev_b32_e32 v66, 1, v66
	v_cvt_pk_bf16_f32 v50, v50, v51
	v_mul_f32_e32 v51, v67, v54
	v_lshl_add_u64 v[64:65], s[6:7], 0, v[64:65]
	v_and_b32_e32 v128, 16, v66
	v_mul_f32_e32 v52, v67, v55
	v_cvt_pk_bf16_f32 v51, v51, v52
	v_lshl_add_u64 v[64:65], v[64:65], 0, v[128:129]
	v_permlane32_swap_b32_e32 v48, v50
	v_permlane32_swap_b32_e32 v49, v51
	global_store_dwordx4 v[64:65], v[48:51], off
	v_mfma_f32_32x32x16_bf16 v[0:15], v[86:89], v[70:73], v[0:15]
	v_mul_f32_e32 v52, v67, v63
	v_mul_f32_e32 v48, v67, v56
	v_mul_f32_e32 v49, v67, v57
	v_cvt_pk_bf16_f32 v48, v48, v49
	v_mul_f32_e32 v49, v67, v58
	v_mul_f32_e32 v50, v67, v59
	v_cvt_pk_bf16_f32 v49, v49, v50
	v_mul_f32_e32 v50, v67, v60
	v_mul_f32_e32 v51, v67, v61
	v_cvt_pk_bf16_f32 v50, v50, v51
	v_mul_f32_e32 v51, v67, v62
	v_cvt_pk_bf16_f32 v51, v51, v52
	v_permlane32_swap_b32_e32 v48, v50
	s_nop 0
	v_permlane32_swap_b32_e32 v49, v51
	v_mul_f32_e32 v32, v67, v32
	v_mul_f32_e32 v33, v67, v33
	global_store_dwordx4 v[64:65], v[48:51], off offset:32
	v_cvt_pk_bf16_f32 v32, v32, v33
	v_mul_f32_e32 v33, v67, v34
	v_mul_f32_e32 v34, v67, v35
	v_cvt_pk_bf16_f32 v33, v33, v34
	v_mul_f32_e32 v34, v67, v36
	v_mul_f32_e32 v35, v67, v37
	v_cvt_pk_bf16_f32 v34, v34, v35
	v_mul_f32_e32 v35, v67, v38
	v_mul_f32_e32 v36, v67, v39
	v_cvt_pk_bf16_f32 v35, v35, v36
	v_permlane32_swap_b32_e32 v32, v34
	v_permlane32_swap_b32_e32 v33, v35
	v_mfma_f32_32x32x16_bf16 v[0:15], v[90:93], v[74:77], v[0:15]
	global_store_dwordx4 v[64:65], v[32:35], off offset:64
	v_mul_f32_e32 v36, v67, v47
	v_mul_f32_e32 v16, v67, v16
	v_mul_f32_e32 v32, v67, v40
	v_mul_f32_e32 v33, v67, v41
	v_cvt_pk_bf16_f32 v32, v32, v33
	v_mul_f32_e32 v33, v67, v42
	v_mul_f32_e32 v34, v67, v43
	v_cvt_pk_bf16_f32 v33, v33, v34
	v_mul_f32_e32 v34, v67, v44
	v_mul_f32_e32 v35, v67, v45
	v_cvt_pk_bf16_f32 v34, v34, v35
	v_mul_f32_e32 v35, v67, v46
	v_cvt_pk_bf16_f32 v35, v35, v36
	v_permlane32_swap_b32_e32 v32, v34
	s_nop 0
	v_permlane32_swap_b32_e32 v33, v35
	v_mul_f32_e32 v17, v67, v17
	global_store_dwordx4 v[64:65], v[32:35], off offset:96
	v_cvt_pk_bf16_f32 v16, v16, v17
	v_mul_f32_e32 v17, v67, v18
	v_mul_f32_e32 v18, v67, v19
	v_cvt_pk_bf16_f32 v17, v17, v18
	v_mul_f32_e32 v18, v67, v20
	v_mul_f32_e32 v19, v67, v21
	v_mfma_f32_32x32x16_bf16 v[0:15], v[94:97], v[78:81], v[0:15]
	v_cvt_pk_bf16_f32 v18, v18, v19
	v_mul_f32_e32 v19, v67, v22
	v_mul_f32_e32 v20, v67, v23
	v_cvt_pk_bf16_f32 v19, v19, v20
	v_permlane32_swap_b32_e32 v16, v18
	v_permlane32_swap_b32_e32 v17, v19
	global_store_dwordx4 v[64:65], v[16:19], off offset:128
	v_mul_f32_e32 v20, v67, v31
	s_nop 5
	v_mul_f32_e32 v0, v67, v0
	v_mul_f32_e32 v16, v67, v24
	v_mul_f32_e32 v17, v67, v25
	v_cvt_pk_bf16_f32 v16, v16, v17
	v_mul_f32_e32 v17, v67, v26
	v_mul_f32_e32 v18, v67, v27
	v_cvt_pk_bf16_f32 v17, v17, v18
	v_mul_f32_e32 v18, v67, v28
	v_mul_f32_e32 v19, v67, v29
	v_cvt_pk_bf16_f32 v18, v18, v19
	v_mul_f32_e32 v19, v67, v30
	v_cvt_pk_bf16_f32 v19, v19, v20
	v_permlane32_swap_b32_e32 v16, v18
	s_nop 0
	v_permlane32_swap_b32_e32 v17, v19
	v_mul_f32_e32 v1, v67, v1
	global_store_dwordx4 v[64:65], v[16:19], off offset:160
	v_cvt_pk_bf16_f32 v0, v0, v1
	v_mul_f32_e32 v1, v67, v2
	v_mul_f32_e32 v2, v67, v3
	v_cvt_pk_bf16_f32 v1, v1, v2
	v_mul_f32_e32 v2, v67, v4
	v_mul_f32_e32 v3, v67, v5
	v_cvt_pk_bf16_f32 v2, v2, v3
	v_mul_f32_e32 v3, v67, v6
	v_mul_f32_e32 v4, v67, v7
	v_cvt_pk_bf16_f32 v3, v3, v4
	v_permlane32_swap_b32_e32 v0, v2
	v_permlane32_swap_b32_e32 v1, v3
	global_store_dwordx4 v[64:65], v[0:3], off offset:192
	v_mul_f32_e32 v4, v67, v15
	s_mov_b64 s[6:7], 0
	v_mul_f32_e32 v0, v67, v8
	v_mul_f32_e32 v1, v67, v9
	v_cvt_pk_bf16_f32 v0, v0, v1
	v_mul_f32_e32 v1, v67, v10
	v_mul_f32_e32 v2, v67, v11
	v_cvt_pk_bf16_f32 v1, v1, v2
	v_mul_f32_e32 v2, v67, v12
	v_mul_f32_e32 v3, v67, v13
	v_cvt_pk_bf16_f32 v2, v2, v3
	v_mul_f32_e32 v3, v67, v14
	v_cvt_pk_bf16_f32 v3, v3, v4
	v_permlane32_swap_b32_e32 v0, v2
	s_nop 0
	v_permlane32_swap_b32_e32 v1, v3
	global_store_dwordx4 v[64:65], v[0:3], off offset:224

.LBB0_814:
	s_add_i32 s24, s23, -3
	ds_read_b128 v[64:67], v198 offset:49152
	ds_read_b128 v[68:71], v198 offset:57344
	ds_read_b128 v[212:215], v200 offset:49152
	ds_read_b128 v[216:219], v200 offset:57344
	v_exp_f32_e32 v160, v160
	v_exp_f32_e32 v161, v161
	s_waitcnt lgkmcnt(3)
	v_mfma_f32_32x32x16_bf16 v[80:95], v[64:67], v[120:123], 0
	v_exp_f32_e32 v152, v152
	v_exp_f32_e32 v153, v153
	v_exp_f32_e32 v158, v158
	v_exp_f32_e32 v150, v150
	v_exp_f32_e32 v159, v159
	v_exp_f32_e32 v151, v151
	v_exp_f32_e32 v156, v156
	s_waitcnt lgkmcnt(2)
	v_mfma_f32_32x32x16_bf16 v[64:79], v[68:71], v[120:123], 0
	v_exp_f32_e32 v148, v148
	v_exp_f32_e32 v157, v157
	v_exp_f32_e32 v149, v149
	v_add_f32_e32 v162, v176, v211
	v_add_f32_e32 v180, v166, v173
	v_add_f32_e32 v194, v160, v161
	v_add_f32_e32 v195, v152, v153
	s_waitcnt lgkmcnt(1)
	v_mfma_f32_32x32x16_bf16 v[80:95], v[212:215], v[124:127], v[80:95]
	v_exp_f32_e32 v154, v154
	v_exp_f32_e32 v146, v146
	v_add_f32_e32 v162, v163, v162
	v_add_f32_e32 v180, v167, v180
	v_add_f32_e32 v194, v158, v194
	v_add_f32_e32 v195, v150, v195
	v_exp_f32_e32 v155, v155
	s_waitcnt lgkmcnt(0)
	v_mfma_f32_32x32x16_bf16 v[64:79], v[216:219], v[124:127], v[64:79]
	ds_read_b128 v[212:215], v199 offset:49152
	ds_read_b128 v[216:219], v199 offset:57344
	v_exp_f32_e32 v147, v147
	v_add_f32_e32 v162, v177, v162
	v_add_f32_e32 v180, v172, v180
	v_add_f32_e32 v194, v159, v194
	v_add_f32_e32 v195, v151, v195
	v_add_f32_e32 v162, v164, v162
	s_waitcnt lgkmcnt(1)
	v_mfma_f32_32x32x16_bf16 v[80:95], v[212:215], v[116:119], v[80:95]
	v_add_f32_e32 v180, v168, v180
	v_add_f32_e32 v194, v156, v194
	v_add_f32_e32 v195, v148, v195
	v_add_f32_e32 v162, v175, v162
	v_add_f32_e32 v180, v171, v180
	v_add_f32_e32 v194, v157, v194
	v_add_f32_e32 v195, v149, v195
	s_waitcnt lgkmcnt(0)
	v_mfma_f32_32x32x16_bf16 v[64:79], v[216:219], v[116:119], v[64:79]
	ds_read_b128 v[212:215], v193 offset:49152
	ds_read_b128 v[216:219], v193 offset:57344
	v_add_f32_e32 v162, v165, v162
	v_add_f32_e32 v180, v169, v180
	v_add_f32_e32 v194, v154, v194
	v_add_f32_e32 v195, v146, v195
	v_add_f32_e32 v162, v174, v162
	s_waitcnt lgkmcnt(1)
	v_mfma_f32_32x32x16_bf16 v[80:95], v[212:215], v[112:115], v[80:95]
	v_add_f32_e32 v180, v170, v180
	v_add_f32_e32 v194, v155, v194
	v_add_f32_e32 v195, v147, v195
	v_add_f32_e32 v162, v180, v162
	v_add_f32_e32 v180, v195, v194
	v_add_f32_e32 v209, v162, v180
	s_waitcnt lgkmcnt(0)
	v_mfma_f32_32x32x16_bf16 v[64:79], v[216:219], v[112:115], v[64:79]
	ds_read_b128 v[212:215], v192 offset:49152
	ds_read_b128 v[216:219], v192 offset:57344
	s_waitcnt lgkmcnt(1)
	v_mfma_f32_32x32x16_bf16 v[80:95], v[212:215], v[108:111], v[80:95]
	s_waitcnt lgkmcnt(0)
	v_mfma_f32_32x32x16_bf16 v[64:79], v[216:219], v[108:111], v[64:79]
	ds_read_b128 v[212:215], v191 offset:49152
	ds_read_b128 v[216:219], v191 offset:57344
	s_waitcnt lgkmcnt(1)
	v_mfma_f32_32x32x16_bf16 v[80:95], v[212:215], v[104:107], v[80:95]
	s_waitcnt lgkmcnt(0)
	v_mfma_f32_32x32x16_bf16 v[64:79], v[216:219], v[104:107], v[64:79]
	ds_read_b128 v[212:215], v190 offset:49152
	ds_read_b128 v[216:219], v190 offset:57344
	s_waitcnt lgkmcnt(1)
	v_mfma_f32_32x32x16_bf16 v[80:95], v[212:215], v[100:103], v[80:95]
	s_waitcnt lgkmcnt(0)
	v_mfma_f32_32x32x16_bf16 v[64:79], v[216:219], v[100:103], v[64:79]
	ds_read_b128 v[212:215], v189 offset:49152
	ds_read_b128 v[216:219], v189 offset:57344
	v_cvt_pk_bf16_f32 v162, v176, v211
	v_cvt_pk_bf16_f32 v163, v163, v177
	v_cvt_pk_bf16_f32 v164, v164, v175
	v_cvt_pk_bf16_f32 v165, v165, v174
	v_cvt_pk_bf16_f32 v166, v166, v173
	v_cvt_pk_bf16_f32 v167, v167, v172
	s_waitcnt lgkmcnt(1)
	v_mfma_f32_32x32x16_bf16 v[80:95], v[212:215], v[96:99], v[80:95]
	v_cvt_pk_bf16_f32 v168, v168, v171
	v_cvt_pk_bf16_f32 v169, v169, v170
	v_cvt_pk_bf16_f32 v170, v160, v161
	v_cvt_pk_bf16_f32 v171, v158, v159
	v_cvt_pk_bf16_f32 v172, v156, v157
	v_cvt_pk_bf16_f32 v173, v154, v155
	v_cvt_pk_bf16_f32 v174, v152, v153
	s_waitcnt lgkmcnt(0)
	v_mfma_f32_32x32x16_bf16 v[64:79], v[216:219], v[96:99], v[64:79]
	v_cvt_pk_bf16_f32 v175, v150, v151
	v_cvt_pk_bf16_f32 v176, v148, v149
	v_cvt_pk_bf16_f32 v177, v146, v147
	s_cmp_gt_u32 s24, 1
	s_mov_b64 s[10:11], -1
	s_cbranch_scc0 .LBB0_816
	s_add_i32 s25, s17, s23
	s_add_i32 s2, s25, -5
	s_min_i32 s2, s2, s18
	s_lshl_b32 s2, s2, 6
	s_addk_i32 s2, 0x100
	s_mov_b64 s[10:11], 0

.LBB0_825:
	v_cndmask_b32_e64 v206, v65, v206, s[58:59]
	v_mul_f32_e32 v138, 0xbe0293ee, v206
	v_fmamk_f32 v65, v162, 0x3e0293ee, v138
	v_fmamk_f32 v66, v163, 0x3e0293ee, v138
	v_fmamk_f32 v67, v164, 0x3e0293ee, v138
	v_fmamk_f32 v68, v165, 0x3e0293ee, v138
	v_fmamk_f32 v69, v166, 0x3e0293ee, v138
	v_fmamk_f32 v70, v167, 0x3e0293ee, v138
	v_fmamk_f32 v73, v168, 0x3e0293ee, v138
	v_fmamk_f32 v74, v169, 0x3e0293ee, v138
	v_fmamk_f32 v75, v170, 0x3e0293ee, v138
	v_fmamk_f32 v76, v171, 0x3e0293ee, v138
	v_fmamk_f32 v77, v172, 0x3e0293ee, v138
	v_fmamk_f32 v78, v173, 0x3e0293ee, v138
	v_fmamk_f32 v80, v174, 0x3e0293ee, v138
	v_fmamk_f32 v81, v175, 0x3e0293ee, v138
	v_fmamk_f32 v82, v176, 0x3e0293ee, v138
	v_fmamk_f32 v83, v177, 0x3e0293ee, v138
	v_exp_f32_e32 v170, v65
	v_exp_f32_e32 v171, v66
	v_exp_f32_e32 v172, v67
	v_exp_f32_e32 v173, v68
	v_exp_f32_e32 v174, v69
	v_exp_f32_e32 v175, v70
	v_exp_f32_e32 v176, v73
	v_exp_f32_e32 v177, v74
	v_fmamk_f32 v162, v71, 0x3e0293ee, v138
	v_fmamk_f32 v163, v72, 0x3e0293ee, v138
	v_fmamk_f32 v164, v217, 0x3e0293ee, v138
	v_fmamk_f32 v165, v218, 0x3e0293ee, v138
	v_fmamk_f32 v166, v219, 0x3e0293ee, v138
	v_fmamk_f32 v167, v220, 0x3e0293ee, v138
	v_fmamk_f32 v168, v221, 0x3e0293ee, v138
	v_fmamk_f32 v169, v222, 0x3e0293ee, v138
	v_fmamk_f32 v139, v64, 0x3e0293ee, v138
	v_fmamk_f32 v140, v211, 0x3e0293ee, v138
	v_fmamk_f32 v141, v212, 0x3e0293ee, v138
	v_fmamk_f32 v142, v213, 0x3e0293ee, v138
	v_fmamk_f32 v143, v214, 0x3e0293ee, v138
	v_fmamk_f32 v144, v215, 0x3e0293ee, v138
	v_fmamk_f32 v145, v216, 0x3e0293ee, v138
	v_fmac_f32_e32 v138, 0x3e0293ee, v79
	v_exp_f32_e32 v194, v75
	v_exp_f32_e32 v195, v76
	v_exp_f32_e32 v196, v77
	v_exp_f32_e32 v197, v78
	v_exp_f32_e32 v211, v80
	v_exp_f32_e32 v214, v81
	v_exp_f32_e32 v215, v82
	v_exp_f32_e32 v216, v83
	s_waitcnt lgkmcnt(0)
	s_barrier
	ds_read_b128 v[64:67], v198 offset:32768
	ds_read_b128 v[68:71], v198 offset:40960
	ds_read_b128 v[130:133], v200 offset:32768
	ds_read_b128 v[134:137], v200 offset:40960
	v_exp_f32_e32 v138, v138
	s_waitcnt lgkmcnt(3)
	v_mfma_f32_32x32x16_bf16 v[80:95], v[64:67], v[120:123], 0
	s_waitcnt lgkmcnt(2)
	v_mfma_f32_32x32x16_bf16 v[64:79], v[68:71], v[120:123], 0
	s_waitcnt lgkmcnt(1)
	v_mfma_f32_32x32x16_bf16 v[80:95], v[130:133], v[124:127], v[80:95]
	s_waitcnt lgkmcnt(0)
	v_mfma_f32_32x32x16_bf16 v[64:79], v[134:137], v[124:127], v[64:79]
	ds_read_b128 v[130:133], v199 offset:32768
	ds_read_b128 v[134:137], v199 offset:40960
	s_waitcnt lgkmcnt(1)
	v_mfma_f32_32x32x16_bf16 v[80:95], v[130:133], v[116:119], v[80:95]
	s_waitcnt lgkmcnt(0)
	v_mfma_f32_32x32x16_bf16 v[64:79], v[134:137], v[116:119], v[64:79]
	ds_read_b128 v[130:133], v193 offset:32768
	ds_read_b128 v[134:137], v193 offset:40960
	s_waitcnt lgkmcnt(1)
	v_mfma_f32_32x32x16_bf16 v[80:95], v[130:133], v[112:115], v[80:95]
	s_waitcnt lgkmcnt(0)
	v_mfma_f32_32x32x16_bf16 v[64:79], v[134:137], v[112:115], v[64:79]
	ds_read_b128 v[130:133], v192 offset:32768
	ds_read_b128 v[134:137], v192 offset:40960
	s_waitcnt lgkmcnt(1)
	v_mfma_f32_32x32x16_bf16 v[80:95], v[130:133], v[108:111], v[80:95]
	s_waitcnt lgkmcnt(0)
	v_mfma_f32_32x32x16_bf16 v[64:79], v[134:137], v[108:111], v[64:79]
	ds_read_b128 v[130:133], v191 offset:32768
	ds_read_b128 v[134:137], v191 offset:40960
	s_waitcnt lgkmcnt(1)
	v_mfma_f32_32x32x16_bf16 v[80:95], v[130:133], v[104:107], v[80:95]
	s_waitcnt lgkmcnt(0)
	v_mfma_f32_32x32x16_bf16 v[64:79], v[134:137], v[104:107], v[64:79]
	ds_read_b128 v[130:133], v190 offset:32768
	ds_read_b128 v[134:137], v190 offset:40960
	s_waitcnt lgkmcnt(1)
	v_mfma_f32_32x32x16_bf16 v[80:95], v[130:133], v[100:103], v[80:95]
	s_waitcnt lgkmcnt(0)
	v_mfma_f32_32x32x16_bf16 v[64:79], v[134:137], v[100:103], v[64:79]
	ds_read_b128 v[130:133], v189 offset:32768
	ds_read_b128 v[134:137], v189 offset:40960
	s_waitcnt lgkmcnt(1)
	v_mfma_f32_32x32x16_bf16 v[80:95], v[130:133], v[96:99], v[80:95]
	v_exp_f32_e32 v130, v139
	v_exp_f32_e32 v131, v140
	v_exp_f32_e32 v139, v163
	v_exp_f32_e32 v140, v164
	v_exp_f32_e32 v132, v141
	v_exp_f32_e32 v141, v165
	v_exp_f32_e32 v133, v142
	v_exp_f32_e32 v142, v166
	s_waitcnt lgkmcnt(0)
	v_mfma_f32_32x32x16_bf16 v[64:79], v[134:137], v[96:99], v[64:79]
	v_exp_f32_e32 v134, v143
	v_exp_f32_e32 v143, v167
	v_exp_f32_e32 v135, v144
	v_exp_f32_e32 v137, v162
	v_exp_f32_e32 v144, v168
	v_add_f32_e32 v162, v170, v171
	v_add_f32_e32 v163, v194, v195
	v_add_f32_e32 v164, v130, v131
	v_add_f32_e32 v165, v139, v140
	v_exp_f32_e32 v136, v145
	v_exp_f32_e32 v145, v169
	v_add_f32_e32 v162, v172, v162
	v_add_f32_e32 v163, v196, v163
	v_add_f32_e32 v164, v132, v164
	v_add_f32_e32 v165, v141, v165
	v_add_f32_e32 v162, v173, v162
	v_add_f32_e32 v163, v197, v163
	v_add_f32_e32 v164, v133, v164
	v_add_f32_e32 v165, v142, v165
	v_add_f32_e32 v162, v174, v162
	v_add_f32_e32 v163, v211, v163
	v_add_f32_e32 v164, v134, v164
	v_add_f32_e32 v165, v143, v165
	v_add_f32_e32 v162, v175, v162
	v_add_f32_e32 v163, v214, v163
	v_add_f32_e32 v164, v135, v164
	v_add_f32_e32 v165, v144, v165
	v_add_f32_e32 v162, v176, v162
	v_add_f32_e32 v163, v215, v163
	v_add_f32_e32 v164, v136, v164
	v_add_f32_e32 v165, v145, v165
	v_add_f32_e32 v162, v177, v162
	v_add_f32_e32 v163, v216, v163
	v_add_f32_e32 v164, v137, v164
	v_add_f32_e32 v165, v138, v165
	v_add_f32_e32 v162, v163, v162
	v_add_f32_e32 v163, v165, v164
	v_add_f32_e32 v212, v163, v162
	v_cvt_pk_bf16_f32 v162, v170, v171
	v_cvt_pk_bf16_f32 v163, v172, v173
	v_cvt_pk_bf16_f32 v164, v174, v175
	v_cvt_pk_bf16_f32 v165, v176, v177
	v_cvt_pk_bf16_f32 v166, v194, v195
	v_cvt_pk_bf16_f32 v167, v196, v197
	v_cvt_pk_bf16_f32 v168, v211, v214
	v_cvt_pk_bf16_f32 v169, v215, v216
	v_cvt_pk_bf16_f32 v170, v130, v131
	v_cvt_pk_bf16_f32 v171, v132, v133
	v_cvt_pk_bf16_f32 v172, v134, v135
	v_cvt_pk_bf16_f32 v173, v136, v137
	v_cvt_pk_bf16_f32 v174, v139, v140
	v_cvt_pk_bf16_f32 v175, v141, v142
	v_cvt_pk_bf16_f32 v176, v143, v144
	v_cvt_pk_bf16_f32 v177, v145, v138
	s_min_i32 s3, s23, s21
	s_cmp_gt_i32 s3, 3
	s_mov_b64 s[10:11], -1
	s_cbranch_scc0 .LBB0_827
	s_add_i32 s2, s3, s20
	s_min_i32 s2, s2, s18
	s_lshl_b32 s2, s2, 6
	s_addk_i32 s2, 0x100
	s_mov_b64 s[10:11], 0

.LBB0_836:
	v_cndmask_b32_e64 v206, v66, v206, s[58:59]
	v_mul_f32_e32 v66, 0xbe0293ee, v206
	v_mov_b32_e32 v88, v66
	v_fmamk_f32 v67, v163, 0x3e0293ee, v66
	v_fmamk_f32 v68, v172, 0x3e0293ee, v66
	v_fmamk_f32 v69, v173, 0x3e0293ee, v66
	v_fmamk_f32 v74, v174, 0x3e0293ee, v66
	v_fmamk_f32 v75, v175, 0x3e0293ee, v66
	v_fmamk_f32 v76, v176, 0x3e0293ee, v66
	v_fmamk_f32 v77, v177, 0x3e0293ee, v66
	v_fmamk_f32 v80, v211, 0x3e0293ee, v66
	v_fmamk_f32 v81, v214, 0x3e0293ee, v66
	v_fmamk_f32 v82, v215, 0x3e0293ee, v66
	v_fmamk_f32 v83, v216, 0x3e0293ee, v66
	v_fmamk_f32 v84, v217, 0x3e0293ee, v66
	v_fmamk_f32 v85, v218, 0x3e0293ee, v66
	v_fmamk_f32 v86, v219, 0x3e0293ee, v66
	v_fmamk_f32 v87, v221, 0x3e0293ee, v66
	v_fmac_f32_e32 v88, 0x3e0293ee, v220
	v_pk_fma_f32 v[148:149], v[170:171], s[52:53], v[66:67] op_sel_hi:[1,0,0]
	v_pk_fma_f32 v[150:151], v[168:169], s[52:53], v[66:67] op_sel_hi:[1,0,0]
	v_pk_fma_f32 v[156:157], v[166:167], s[52:53], v[66:67] op_sel_hi:[1,0,0]
	v_pk_fma_f32 v[158:159], v[164:165], s[52:53], v[66:67] op_sel_hi:[1,0,0]
	v_exp_f32_e32 v176, v67
	v_exp_f32_e32 v211, v68
	v_exp_f32_e32 v163, v69
	v_exp_f32_e32 v177, v74
	v_exp_f32_e32 v164, v75
	v_exp_f32_e32 v175, v76
	v_exp_f32_e32 v165, v77
	v_exp_f32_e32 v174, v80
	v_exp_f32_e32 v166, v81
	v_exp_f32_e32 v173, v82
	v_exp_f32_e32 v167, v83
	v_exp_f32_e32 v172, v84
	v_exp_f32_e32 v168, v85
	v_exp_f32_e32 v171, v86
	v_exp_f32_e32 v169, v87
	v_exp_f32_e32 v170, v88
	v_pk_fma_f32 v[160:161], v[64:65], s[52:53], v[66:67] op_sel_hi:[1,0,0]
	v_fma_f32 v64, v187, v205, v209
	s_add_i32 s2, s23, 2
	s_addk_i32 s22, 0x80
	v_pk_fma_f32 v[146:147], v[78:79], s[52:53], v[66:67] op_sel_hi:[1,0,0]
	v_pk_fma_f32 v[152:153], v[72:73], s[52:53], v[66:67] op_sel_hi:[1,0,0]
	v_pk_fma_f32 v[154:155], v[70:71], s[52:53], v[66:67] op_sel_hi:[1,0,0]
	v_fma_f32 v187, v64, v180, v212
	s_cmp_ge_i32 s23, s19
	v_add_u32_e32 v208, 0xf8, v208
	s_waitcnt lgkmcnt(0)
	s_barrier
	s_cbranch_scc1 .LBB0_839
	s_mov_b32 s23, s2
	v_mov_b32_e32 v205, v162
	s_branch .LBB0_814
